# speedup vs baseline: 1.0019x; 1.0019x over previous
.Lk_228:
	s_and_b64 s[10:11], s[10:11], exec
	s_cselect_b32 s13, s63, s39
	s_cselect_b32 s12, s62, s38
	s_cselect_b32 s11, s65, s41
	s_cselect_b32 s10, s64, s40
	s_lshl_b32 s17, s17, 2
	v_lshl_or_b32 v4, v54, 3, s17
	global_load_dword v6, v4, s[12:13]
	global_load_dword v8, v4, s[10:11]
	global_load_dword v7, v4, s[12:13] offset:256
	global_load_dword v9, v4, s[10:11] offset:256
	global_load_dword v10, v4, s[12:13] offset:512
	global_load_dword v48, v4, s[10:11] offset:512
	global_load_dword v49, v4, s[10:11] offset:768
	global_load_dword v11, v4, s[12:13] offset:768
	global_load_dword v120, v4, s[12:13] offset:4
	global_load_dword v121, v4, s[12:13] offset:260
	global_load_dword v122, v4, s[12:13] offset:516
	global_load_dword v123, v4, s[12:13] offset:772
	global_load_dword v124, v4, s[10:11] offset:4
	global_load_dword v125, v4, s[10:11] offset:260
	global_load_dword v126, v4, s[10:11] offset:516
	global_load_dword v127, v4, s[10:11] offset:772
	v_or_b32_e32 v50, 1, v12
	v_lshlrev_b32_e32 v2, 8, v50
	v_mov_b32_e32 v3, v5
	v_lshl_add_u64 v[2:3], s[8:9], 0, v[2:3]
	v_lshlrev_b32_e32 v44, 2, v1
	v_mov_b32_e32 v45, v5
	v_lshl_add_u64 v[2:3], v[2:3], 0, v[44:45]
	global_load_dwordx4 v[12:15], v[2:3], off offset:16
	global_load_dwordx4 v[40:43], v[2:3], off
	global_load_dwordx4 v[16:19], v[2:3], off offset:144
	global_load_dwordx4 v[36:39], v[2:3], off offset:128
	v_lshlrev_b32_e32 v2, s16, v50
	v_lshlrev_b32_e32 v2, 2, v2
	global_load_dword v45, v2, s[6:7]
	v_mov_b32_e32 v3, v5
	v_lshl_add_u64 v[52:53], s[6:7], 0, v[2:3]
	s_and_b64 vcc, exec, s[0:1]
	v_mov_b32_e32 v50, 0
	s_cbranch_vccz .Lk_291
	v_mov_b32_e32 v55, 0
	s_and_b64 vcc, exec, s[0:1]
	v_mov_b32_e32 v56, 0
	s_cbranch_vccz .Lk_292

.Lk_232:
	s_waitcnt vmcnt(21)
	v_fma_mixlo_f16 v52, v46, v58, 0
	v_fma_mixlo_f16 v53, v46, v58, -v52 op_sel_hi:[0,0,1]
	v_cvt_f16_f32_e32 v58, v57
	v_cmp_eq_u32_e32 vcc, 1, v54
	v_cmp_gt_u32_e64 s[0:1], 16, v80
	v_cvt_f16_f32_e32 v64, v51
	v_cvt_f32_f16_e32 v60, v58
	v_cndmask_b32_e32 v53, 0, v53, vcc
	v_cndmask_b32_e64 v65, v53, v52, s[0:1]
	v_cvt_f32_f16_e32 v61, v64
	v_sub_f32_e32 v53, v57, v60
	v_cvt_f16_f32_e32 v53, v53
	v_cvt_f16_f32_e32 v57, v59
	v_cndmask_b32_e64 v67, 0, v52, s[0:1]
	v_sub_f32_e32 v51, v51, v61
	v_cndmask_b32_e32 v53, 0, v53, vcc
	v_cndmask_b32_e64 v66, v53, v58, s[0:1]
	v_cvt_f32_f16_e32 v53, v57
	v_cndmask_b32_e64 v68, 0, v58, s[0:1]
	s_waitcnt vmcnt(2)
	v_pk_mul_f32 v[16:17], v[46:47], v[16:17] op_sel_hi:[0,1]
	v_pk_mul_f32 v[18:19], v[46:47], v[18:19] op_sel_hi:[0,1]
	v_sub_f32_e32 v52, v59, v53
	v_cvt_f16_f32_e32 v69, v52
	v_mov_b32_e32 v52, v120
	v_mov_b32_e32 v53, v121
	v_mov_b32_e32 v58, v122
	v_mov_b32_e32 v59, v123
	v_mov_b32_e32 v60, v124
	v_mov_b32_e32 v61, v125
	v_mov_b32_e32 v62, v126
	v_mov_b32_e32 v63, v127
	v_pk_mul_f32 v[20:21], v[46:47], v[20:21] op_sel_hi:[0,1]
	v_pk_mul_f32 v[22:23], v[46:47], v[22:23] op_sel_hi:[0,1]
	v_pk_mul_f32 v[24:25], v[46:47], v[24:25] op_sel_hi:[0,1]
	v_pk_mul_f32 v[26:27], v[46:47], v[26:27] op_sel_hi:[0,1]
	v_cvt_pk_f16_f32 v16, v16, v17
	v_cvt_pk_f16_f32 v17, v18, v19
	v_pk_mul_f32 v[18:19], v[46:47], v[32:33] op_sel_hi:[0,1]
	v_pk_mul_f32 v[32:33], v[46:47], v[34:35] op_sel_hi:[0,1]
	v_cvt_pk_f16_f32 v20, v20, v21
	v_cvt_pk_f16_f32 v21, v22, v23
	v_pk_mul_f32 v[22:23], v[46:47], v[28:29] op_sel_hi:[0,1]
	v_pk_mul_f32 v[28:29], v[46:47], v[30:31] op_sel_hi:[0,1]
	v_cvt_pk_f16_f32 v24, v24, v25
	v_cvt_pk_f16_f32 v25, v26, v27
	v_cvt_f16_f32_e32 v26, v50
	v_cvt_pk_f16_f32 v18, v18, v19
	v_cvt_pk_f16_f32 v19, v32, v33
	v_cvt_pk_f16_f32 v22, v22, v23
	v_cvt_pk_f16_f32 v23, v28, v29
	v_cvt_f16_f32_e32 v29, v56
	v_cvt_f16_f32_e32 v32, v55
	v_cvt_f32_f16_e32 v30, v26
	v_cvt_f16_f32_e32 v51, v51
	v_cvt_f32_f16_e32 v31, v29
	v_cvt_f32_f16_e32 v33, v32
	v_sub_f32_e32 v30, v50, v30
	v_cvt_f16_f32_e32 v30, v30
	v_sub_f32_e32 v31, v56, v31
	v_sub_f32_e32 v33, v55, v33
	v_cvt_f16_f32_e32 v31, v31
	v_cvt_f16_f32_e32 v33, v33
	v_pk_mul_f32 v[12:13], v[46:47], v[12:13] op_sel_hi:[0,1]
	v_pk_mul_f32 v[14:15], v[46:47], v[14:15] op_sel_hi:[0,1]
	s_waitcnt vmcnt(0)
	v_fma_mixlo_f16 v27, v46, v45, 0
	v_cvt_pk_f16_f32 v12, v12, v13
	v_cvt_pk_f16_f32 v13, v14, v15
	v_pk_mul_f32 v[14:15], v[46:47], v[36:37] op_sel_hi:[0,1]
	v_pk_mul_f32 v[36:37], v[46:47], v[38:39] op_sel_hi:[0,1]
	v_fma_mixlo_f16 v28, v46, v45, -v27 op_sel_hi:[0,0,1]
	v_cndmask_b32_e32 v30, 0, v30, vcc
	v_cvt_pk_f16_f32 v14, v14, v15
	v_cvt_pk_f16_f32 v15, v36, v37
	v_cndmask_b32_e32 v28, 0, v28, vcc
	v_cndmask_b32_e64 v30, v30, v26, s[0:1]
	v_cndmask_b32_e32 v31, 0, v31, vcc
	v_cndmask_b32_e64 v36, 0, v26, s[0:1]
	v_cndmask_b32_e32 v26, 0, v33, vcc
	v_cndmask_b32_e32 v51, 0, v51, vcc
	v_cndmask_b32_e32 v2, 0, v69, vcc
	s_mov_b32 s8, 0x4038aa3b
	v_and_b32_e32 v34, 15, v0
	v_cndmask_b32_e64 v28, v28, v27, s[0:1]
	v_cndmask_b32_e64 v31, v31, v29, s[0:1]
	v_cndmask_b32_e64 v35, 0, v27, s[0:1]
	v_cndmask_b32_e64 v26, v26, v32, s[0:1]
	v_cndmask_b32_e64 v51, v51, v64, s[0:1]
	v_cndmask_b32_e64 v4, 0, v64, s[0:1]
	v_cndmask_b32_e64 v5, 0, v57, s[0:1]
	v_cndmask_b32_e64 v2, v2, v57, s[0:1]
	s_mov_b32 s9, 0xbfb8aa3b
	v_cndmask_b32_e64 v29, 0, v29, s[0:1]
	v_cndmask_b32_e64 v33, 0, v32, s[0:1]
	v_pack_b32_f16 v27, v31, v26
	v_pack_b32_f16 v26, v28, v30
	v_pack_b32_f16 v28, v35, v36
	s_lshl_b32 s0, s15, 8
	v_lshlrev_b32_e32 v81, 4, v34
	v_lshlrev_b32_e32 v35, 2, v54
	s_mov_b32 s7, 0
	v_pk_add_f32 v[6:7], v[6:7], v[8:9]
	v_pk_add_f32 v[8:9], v[10:11], v[48:49]
	s_mov_b32 s6, s9
	v_pk_mul_f32 v[10:11], v[46:47], v[40:41] op_sel_hi:[0,1]
	v_pk_mul_f32 v[40:41], v[46:47], v[42:43] op_sel_hi:[0,1]
	v_pack_b32_f16 v29, v29, v33
	v_lshlrev_b32_e32 v74, 4, v80
	v_or3_b32 v35, v81, v35, s0
	s_waitcnt vmcnt(2)
	v_pk_add_f32 v[30:31], v[52:53], v[60:61]
	v_pack_b32_f16 v3, v51, v2
	s_waitcnt vmcnt(0)
	v_pk_add_f32 v[32:33], v[58:59], v[62:63]
	v_pack_b32_f16 v2, v65, v66
	v_pack_b32_f16 v5, v4, v5
	v_pack_b32_f16 v4, v67, v68
	v_pk_mul_f32 v[8:9], v[8:9], s[8:9]
	v_pk_mul_f32 v[6:7], v[6:7], s[6:7] op_sel_hi:[1,0]
	v_cvt_pk_f16_f32 v10, v10, v11
	v_cvt_pk_f16_f32 v11, v40, v41
	v_pk_mul_f32 v[32:33], v[32:33], s[8:9]
	v_pk_mul_f32 v[30:31], v[30:31], s[6:7] op_sel_hi:[1,0]
	v_add_u32_e32 v78, 0x23280, v74
	v_add_u32_e32 v79, 0x23280, v35
	s_mov_b64 s[0:1], -1
	s_and_b64 vcc, exec, s[4:5]
	s_waitcnt lgkmcnt(0)
	s_barrier
	s_cbranch_vccz .Lk_298
	s_setprio 0
	v_and_b32_e32 v34, 15, v80
	v_lshrrev_b32_e32 v35, 4, v80
	s_and_b32 s10, s15, 1
	v_lshrrev_b32_e32 v36, 2, v34
	v_and_b32_e32 v37, 3, v34
	v_lshl_add_u32 v36, v36, 3, v37
	s_lshl_b32 s11, s10, 2
	v_add_u32_e32 v36, s11, v36
	v_lshlrev_b32_e32 v36, 9, v36
	v_lshl_add_u32 v36, v35, 5, v36
	global_load_dwordx4 v[44:47], v36, s[42:43] offset:0
	global_load_dwordx4 v[48:51], v36, s[42:43] offset:16
	global_load_dwordx4 v[52:55], v36, s[42:43] offset:128
	global_load_dwordx4 v[56:59], v36, s[42:43] offset:144
	global_load_dwordx4 v[60:63], v36, s[42:43] offset:256
	global_load_dwordx4 v[64:67], v36, s[42:43] offset:272
	global_load_dwordx4 v[68:71], v36, s[42:43] offset:384
	global_load_dwordx4 v[72:75], v36, s[42:43] offset:400
	v_lshlrev_b32_e32 v37, 5, v35
	s_lshl_b32 s12, s10, 4
	v_add_u32_e32 v37, s12, v37
	global_load_dwordx4 v[120:123], v37, s[44:45]
	s_mul_i32 s12, s3, 0x70800
	s_add_u32 s16, s22, s12
	s_addc_u32 s17, s23, 0
	s_lshl_b32 s12, s3, 8
	s_add_u32 s18, s24, s12
	s_addc_u32 s19, s25, 0
	s_add_u32 s18, s18, s11
	s_addc_u32 s19, s19, 0
	v_lshlrev_b32_e32 v38, 4, v80
	s_lshl_b32 s12, s10, 3
	v_add_u32_e32 v38, s12, v38
	v_lshlrev_b32_e32 v39, 2, v34
	v_add_u32_e32 v39, 0x1c200, v39
	s_mov_b32 s0, 0x4038aa3b
	s_mov_b32 s1, 0
	s_mov_b32 s9, 2
	s_waitcnt vmcnt(0)
	v_cvt_pk_f16_f32 v104, v44, v45
	v_cvt_pk_f16_f32 v105, v46, v47
	v_cvt_pk_f16_f32 v106, v48, v49
	v_cvt_pk_f16_f32 v107, v50, v51
	v_cvt_pk_f16_f32 v108, v52, v53
	v_cvt_pk_f16_f32 v109, v54, v55
	v_cvt_pk_f16_f32 v110, v56, v57
	v_cvt_pk_f16_f32 v111, v58, v59
	v_cvt_pk_f16_f32 v112, v60, v61
	v_cvt_pk_f16_f32 v113, v62, v63
	v_cvt_pk_f16_f32 v114, v64, v65
	v_cvt_pk_f16_f32 v115, v66, v67
	v_cvt_pk_f16_f32 v116, v68, v69
	v_cvt_pk_f16_f32 v117, v70, v71
	v_cvt_pk_f16_f32 v118, v72, v73
	v_cvt_pk_f16_f32 v119, v74, v75
	ds_read_b32 v64, v39
	v_mov_b32_e32 v40, 0
	v_mov_b32_e32 v41, 0
	v_mov_b32_e32 v61, 0
	v_mov_b32_e32 v63, 0
	v_mov_b32_e32 v83, 0
	v_mov_b32_e32 v58, 0xc038aa3b
	v_mov_b32_e32 v59, 0xc038aa3b
	s_waitcnt lgkmcnt(0)
	v_and_b32_e32 v60, 0xffff, v64
	v_lshrrev_b32_e32 v62, 16, v64
	s_nop 1
	v_mfma_f32_16x16x32_f16 v[50:53], v[2:5], v[60:63], v[6:9]
	v_mfma_f32_16x16x32_f16 v[54:57], v[26:29], v[60:63], v[30:33]
	ds_read_b128 v[42:45], v78 offset:6144
	ds_read_b128 v[46:49], v78 offset:7168
	s_waitcnt lgkmcnt(1)
	v_mfma_f32_16x16x32_f16 v[50:53], v[18:21], v[42:45], v[50:53]
	v_mfma_f32_16x16x32_f16 v[54:57], v[10:13], v[42:45], v[54:57]
	s_waitcnt lgkmcnt(0)
	v_mfma_f32_16x16x32_f16 v[50:53], v[22:25], v[46:49], v[50:53]
	v_mfma_f32_16x16x32_f16 v[54:57], v[14:17], v[46:49], v[54:57]
	ds_read_b32 v64, v39 offset:64
	s_nop 7
	v_exp_f32_e32 v84, v52
	v_exp_f32_e32 v85, v56
	v_exp_f32_e32 v86, v50
	v_exp_f32_e32 v87, v54
	v_exp_f32_e32 v88, v51
	v_exp_f32_e32 v89, v55
	v_pk_add_f32 v[90:91], v[84:85], 1.0 op_sel_hi:[1,0]
	v_pk_fma_f32 v[92:93], v[84:85], s[0:1], v[58:59] op_sel_hi:[1,0,0]
	v_pk_fma_f32 v[90:91], v[86:87], v[90:91], v[90:91]
	v_pk_fma_f32 v[94:95], v[90:91], v[88:89], v[90:91]
	v_rcp_f32_e32 v94, v94
	v_rcp_f32_e32 v95, v95
	v_pk_fma_f32 v[92:93], v[92:93], v[88:89], v[92:93]
	v_pk_fma_f32 v[92:93], v[40:41], v[90:91], v[92:93]
	v_exp_f32_e32 v96, v53
	v_pk_mul_f32 v[40:41], v[92:93], v[94:95]
	v_exp_f32_e32 v98, v40
	v_exp_f32_e32 v99, v41
	v_exp_f32_e32 v97, v57
	v_pk_add_f32 v[100:101], v[98:99], 1.0 op_sel_hi:[1,0]
	v_pk_fma_f32 v[100:101], v[100:101], v[96:97], v[100:101]
	v_rcp_f32_e32 v100, v100
	v_rcp_f32_e32 v101, v101
	v_pk_add_f32 v[102:103], v[98:99], -1.0 op_sel_hi:[1,0]
	v_pk_mul_f32 v[102:103], v[102:103], v[100:101]
	v_cvt_pk_f16_f32 v126, v102, v103
	ds_write_b32 v79, v126 offset:4096
	s_waitcnt lgkmcnt(1)
	v_and_b32_e32 v60, 0xffff, v64
	v_lshrrev_b32_e32 v62, 16, v64
	s_nop 1
	v_mfma_f32_16x16x32_f16 v[50:53], v[2:5], v[60:63], v[6:9]
	v_mfma_f32_16x16x32_f16 v[54:57], v[26:29], v[60:63], v[30:33]
	s_waitcnt lgkmcnt(0)
	s_barrier
	s_cmp_lt_u32 s15, 2
	s_cbranch_scc0 .Lpb_nc_1
	ds_read_b128 v[66:69], v78 offset:0
	ds_read_b128 v[70:73], v78 offset:1024
